# P1 epilogue: straight-line path for plain column tiles (64 cvt_pk + 16 nt stores from the accumulators)
# baseline (speedup 1.0000x reference)
.LBB0_192:
	s_cmp_lt_i32 s6, 36
	s_cbranch_scc0 .Lep_slow
	s_and_b32 s98, s6, -4
	s_cmp_eq_u32 s98, 8
	s_cbranch_scc1 .Lep_slow
	s_add_i32 s98, s6, -12
	s_cmp_lt_u32 s98, 16
	s_cbranch_scc0 .Lep_fast
	s_and_b64 vcc, exec, s[14:15]
	s_cbranch_vccnz .Lep_slow
.Lep_fast:
	v_lshl_add_u32 v200, s4, 8, v192
	v_mov_b64_e32 v[202:203], s[10:11]
	s_lshl_b32 s98, s6, 8
	v_mad_i64_i32 v[202:203], vcc, v200, s84, v[202:203]
	v_or_b32_e32 v204, s98, v198
	v_mov_b32_e32 v205, 0
	v_lshl_add_u64 v[202:203], v[204:205], 1, v[202:203]
	s_mov_b32 s98, 0x68000
	s_mov_b32 s99, 0
	v_cvt_pk_bf16_f32 v208, v124, v125
	v_cvt_pk_bf16_f32 v209, v126, v127
	v_cvt_pk_bf16_f32 v210, v120, v121
	v_cvt_pk_bf16_f32 v211, v122, v123
	global_store_dwordx4 v[202:203], v[208:211], off nt
	v_cvt_pk_bf16_f32 v212, v116, v117
	v_cvt_pk_bf16_f32 v213, v118, v119
	v_cvt_pk_bf16_f32 v214, v112, v113
	v_cvt_pk_bf16_f32 v215, v114, v115
	global_store_dwordx4 v[202:203], v[212:215], off offset:256 nt
	v_lshl_add_u64 v[202:203], v[202:203], 0, s[98:99]
	v_cvt_pk_bf16_f32 v208, v108, v109
	v_cvt_pk_bf16_f32 v209, v110, v111
	v_cvt_pk_bf16_f32 v210, v104, v105
	v_cvt_pk_bf16_f32 v211, v106, v107
	global_store_dwordx4 v[202:203], v[208:211], off nt
	v_cvt_pk_bf16_f32 v212, v100, v101
	v_cvt_pk_bf16_f32 v213, v102, v103
	v_cvt_pk_bf16_f32 v214, v96, v97
	v_cvt_pk_bf16_f32 v215, v98, v99
	global_store_dwordx4 v[202:203], v[212:215], off offset:256 nt
	v_lshl_add_u64 v[202:203], v[202:203], 0, s[98:99]
	v_cvt_pk_bf16_f32 v208, v92, v93
	v_cvt_pk_bf16_f32 v209, v94, v95
	v_cvt_pk_bf16_f32 v210, v88, v89
	v_cvt_pk_bf16_f32 v211, v90, v91
	global_store_dwordx4 v[202:203], v[208:211], off nt
	v_cvt_pk_bf16_f32 v212, v84, v85
	v_cvt_pk_bf16_f32 v213, v86, v87
	v_cvt_pk_bf16_f32 v214, v80, v81
	v_cvt_pk_bf16_f32 v215, v82, v83
	global_store_dwordx4 v[202:203], v[212:215], off offset:256 nt
	v_lshl_add_u64 v[202:203], v[202:203], 0, s[98:99]
	v_cvt_pk_bf16_f32 v208, v76, v77
	v_cvt_pk_bf16_f32 v209, v78, v79
	v_cvt_pk_bf16_f32 v210, v72, v73
	v_cvt_pk_bf16_f32 v211, v74, v75
	global_store_dwordx4 v[202:203], v[208:211], off nt
	v_cvt_pk_bf16_f32 v212, v68, v69
	v_cvt_pk_bf16_f32 v213, v70, v71
	v_cvt_pk_bf16_f32 v214, v64, v65
	v_cvt_pk_bf16_f32 v215, v66, v67
	global_store_dwordx4 v[202:203], v[212:215], off offset:256 nt
	s_mov_b32 s98, 0x208000
	v_lshl_add_u64 v[202:203], v[202:203], 0, s[98:99]
	s_mov_b32 s98, 0x68000
	v_cvt_pk_bf16_f32 v208, v60, v61
	v_cvt_pk_bf16_f32 v209, v62, v63
	v_cvt_pk_bf16_f32 v210, v56, v57
	v_cvt_pk_bf16_f32 v211, v58, v59
	global_store_dwordx4 v[202:203], v[208:211], off nt
	v_cvt_pk_bf16_f32 v212, v52, v53
	v_cvt_pk_bf16_f32 v213, v54, v55
	v_cvt_pk_bf16_f32 v214, v48, v49
	v_cvt_pk_bf16_f32 v215, v50, v51
	global_store_dwordx4 v[202:203], v[212:215], off offset:256 nt
	v_lshl_add_u64 v[202:203], v[202:203], 0, s[98:99]
	v_cvt_pk_bf16_f32 v208, v44, v45
	v_cvt_pk_bf16_f32 v209, v46, v47
	v_cvt_pk_bf16_f32 v210, v40, v41
	v_cvt_pk_bf16_f32 v211, v42, v43
	global_store_dwordx4 v[202:203], v[208:211], off nt
	v_cvt_pk_bf16_f32 v212, v36, v37
	v_cvt_pk_bf16_f32 v213, v38, v39
	v_cvt_pk_bf16_f32 v214, v32, v33
	v_cvt_pk_bf16_f32 v215, v34, v35
	global_store_dwordx4 v[202:203], v[212:215], off offset:256 nt
	v_lshl_add_u64 v[202:203], v[202:203], 0, s[98:99]
	v_cvt_pk_bf16_f32 v208, v28, v29
	v_cvt_pk_bf16_f32 v209, v30, v31
	v_cvt_pk_bf16_f32 v210, v24, v25
	v_cvt_pk_bf16_f32 v211, v26, v27
	global_store_dwordx4 v[202:203], v[208:211], off nt
	v_cvt_pk_bf16_f32 v212, v20, v21
	v_cvt_pk_bf16_f32 v213, v22, v23
	v_cvt_pk_bf16_f32 v214, v16, v17
	v_cvt_pk_bf16_f32 v215, v18, v19
	global_store_dwordx4 v[202:203], v[212:215], off offset:256 nt
	v_lshl_add_u64 v[202:203], v[202:203], 0, s[98:99]
	v_cvt_pk_bf16_f32 v208, v12, v13
	v_cvt_pk_bf16_f32 v209, v14, v15
	v_cvt_pk_bf16_f32 v210, v8, v9
	v_cvt_pk_bf16_f32 v211, v10, v11
	global_store_dwordx4 v[202:203], v[208:211], off nt
	v_cvt_pk_bf16_f32 v212, v4, v5
	v_cvt_pk_bf16_f32 v213, v6, v7
	v_cvt_pk_bf16_f32 v214, v0, v1
	v_cvt_pk_bf16_f32 v215, v2, v3
	global_store_dwordx4 v[202:203], v[212:215], off offset:256 nt
	s_andn2_b64 vcc, exec, s[2:3]
	s_mov_b64 s[2:3], -1
	s_cbranch_vccnz .LBB0_185
	s_branch .LBB0_338
